# t11_st_sc1nt
# baseline (speedup 1.0000x reference)
.Ljoin:
	s_barrier
	v_mov_b32_e32 v6, 0x6000
	ds_read_b96 v[32:34], v6
	ds_read_b96 v[36:38], v6 offset:16
	ds_read_b96 v[40:42], v6 offset:32
	ds_read_b96 v[44:46], v6 offset:48
	v_add_u32_e32 v56, 0xc00, v3
	v_add_u32_e32 v57, 0x1200, v3
	ds_read2_b32 v[8:9], v3 offset0:0 offset1:1
	ds_read_b32 v24, v3 offset:8
	ds_read2_b32 v[10:11], v3 offset0:192 offset1:193
	ds_read_b32 v25, v3 offset:776
	ds_read2_b32 v[12:13], v4 offset0:0 offset1:1
	ds_read_b32 v26, v4 offset:8
	s_waitcnt lgkmcnt(4)
	v_fma_f32 v60, v8, v32, v44
	v_fma_f32 v61, v8, v33, v45
	v_fma_f32 v62, v8, v34, v46
	v_fmac_f32_e32 v60, v9, v36
	v_fmac_f32_e32 v61, v9, v37
	v_fmac_f32_e32 v62, v9, v38
	v_fmac_f32_e32 v60, v24, v40
	v_fmac_f32_e32 v61, v24, v41
	v_fmac_f32_e32 v62, v24, v42
	ds_write2_b32 v3, v60, v61 offset0:0 offset1:1
	ds_write_b32 v3, v62 offset:8
	ds_read2_b32 v[14:15], v4 offset0:192 offset1:193
	ds_read_b32 v27, v4 offset:776
	s_waitcnt lgkmcnt(6)
	v_fma_f32 v35, v10, v32, v44
	v_fma_f32 v39, v10, v33, v45
	v_fma_f32 v43, v10, v34, v46
	v_fmac_f32_e32 v35, v11, v36
	v_fmac_f32_e32 v39, v11, v37
	v_fmac_f32_e32 v43, v11, v38
	v_fmac_f32_e32 v35, v25, v40
	v_fmac_f32_e32 v39, v25, v41
	v_fmac_f32_e32 v43, v25, v42
	ds_write2_b32 v3, v35, v39 offset0:192 offset1:193
	ds_write_b32 v3, v43 offset:776
	ds_read2_b32 v[16:17], v56 offset0:0 offset1:1
	ds_read_b32 v28, v56 offset:8
	s_waitcnt lgkmcnt(8)
	v_fma_f32 v60, v12, v32, v44
	v_fma_f32 v61, v12, v33, v45
	v_fma_f32 v62, v12, v34, v46
	v_fmac_f32_e32 v60, v13, v36
	v_fmac_f32_e32 v61, v13, v37
	v_fmac_f32_e32 v62, v13, v38
	v_fmac_f32_e32 v60, v26, v40
	v_fmac_f32_e32 v61, v26, v41
	v_fmac_f32_e32 v62, v26, v42
	ds_write2_b32 v4, v60, v61 offset0:0 offset1:1
	ds_write_b32 v4, v62 offset:8
	ds_read2_b32 v[18:19], v56 offset0:192 offset1:193
	ds_read_b32 v29, v56 offset:776
	s_waitcnt lgkmcnt(8)
	v_fma_f32 v35, v14, v32, v44
	v_fma_f32 v39, v14, v33, v45
	v_fma_f32 v43, v14, v34, v46
	v_fmac_f32_e32 v35, v15, v36
	v_fmac_f32_e32 v39, v15, v37
	v_fmac_f32_e32 v43, v15, v38
	v_fmac_f32_e32 v35, v27, v40
	v_fmac_f32_e32 v39, v27, v41
	v_fmac_f32_e32 v43, v27, v42
	ds_write2_b32 v4, v35, v39 offset0:192 offset1:193
	ds_write_b32 v4, v43 offset:776
	ds_read2_b32 v[20:21], v57 offset0:0 offset1:1
	ds_read_b32 v30, v57 offset:8
	s_waitcnt lgkmcnt(8)
	v_fma_f32 v60, v16, v32, v44
	v_fma_f32 v61, v16, v33, v45
	v_fma_f32 v62, v16, v34, v46
	v_fmac_f32_e32 v60, v17, v36
	v_fmac_f32_e32 v61, v17, v37
	v_fmac_f32_e32 v62, v17, v38
	v_fmac_f32_e32 v60, v28, v40
	v_fmac_f32_e32 v61, v28, v41
	v_fmac_f32_e32 v62, v28, v42
	ds_write2_b32 v56, v60, v61 offset0:0 offset1:1
	ds_write_b32 v56, v62 offset:8
	ds_read2_b32 v[22:23], v57 offset0:192 offset1:193
	ds_read_b32 v31, v57 offset:776
	s_waitcnt lgkmcnt(8)
	v_fma_f32 v35, v18, v32, v44
	v_fma_f32 v39, v18, v33, v45
	v_fma_f32 v43, v18, v34, v46
	v_fmac_f32_e32 v35, v19, v36
	v_fmac_f32_e32 v39, v19, v37
	v_fmac_f32_e32 v43, v19, v38
	v_fmac_f32_e32 v35, v29, v40
	v_fmac_f32_e32 v39, v29, v41
	v_fmac_f32_e32 v43, v29, v42
	ds_write2_b32 v56, v35, v39 offset0:192 offset1:193
	ds_write_b32 v56, v43 offset:776
	s_waitcnt lgkmcnt(6)
	v_fma_f32 v60, v20, v32, v44
	v_fma_f32 v61, v20, v33, v45
	v_fma_f32 v62, v20, v34, v46
	v_fmac_f32_e32 v60, v21, v36
	v_fmac_f32_e32 v61, v21, v37
	v_fmac_f32_e32 v62, v21, v38
	v_fmac_f32_e32 v60, v30, v40
	v_fmac_f32_e32 v61, v30, v41
	v_fmac_f32_e32 v62, v30, v42
	ds_write2_b32 v57, v60, v61 offset0:0 offset1:1
	ds_write_b32 v57, v62 offset:8
	s_waitcnt lgkmcnt(4)
	v_fma_f32 v35, v22, v32, v44
	v_fma_f32 v39, v22, v33, v45
	v_fma_f32 v43, v22, v34, v46
	v_fmac_f32_e32 v35, v23, v36
	v_fmac_f32_e32 v39, v23, v37
	v_fmac_f32_e32 v43, v23, v38
	v_fmac_f32_e32 v35, v31, v40
	v_fmac_f32_e32 v39, v31, v41
	v_fmac_f32_e32 v43, v31, v42
	ds_write2_b32 v57, v35, v39 offset0:192 offset1:193
	ds_write_b32 v57, v43 offset:776
	ds_read_b128 v[8:11], v2
	ds_read_b128 v[12:15], v2 offset:1024
	ds_read_b128 v[16:19], v2 offset:2048
	ds_read_b128 v[20:23], v2 offset:3072
	ds_read_b128 v[24:27], v2 offset:4096
	ds_read_b128 v[28:31], v2 offset:5120
	s_waitcnt lgkmcnt(5)
	global_store_dwordx4 v1, v[8:11], s[10:11] offset:-2048 sc1 nt
	s_waitcnt lgkmcnt(4)
	global_store_dwordx4 v1, v[12:15], s[10:11] offset:-1024 sc1 nt
	s_waitcnt lgkmcnt(3)
	global_store_dwordx4 v1, v[16:19], s[10:11] offset:0 sc1 nt
	s_waitcnt lgkmcnt(2)
	global_store_dwordx4 v1, v[20:23], s[10:11] offset:1024 sc1 nt
	s_waitcnt lgkmcnt(1)
	global_store_dwordx4 v1, v[24:27], s[10:11] offset:2048 sc1 nt
	s_waitcnt lgkmcnt(0)
	s_and_saveexec_b64 s[16:17], s[14:15]
	global_store_dwordx4 v1, v[28:31], s[10:11] offset:3072 sc1 nt
	s_endpgm
